# baseline (speedup 1.0000x reference)
.LBB5_7:
	s_load_dwordx2 s[2:3], s[0:1], 0x38
	v_lshrrev_b32_e32 v1, 1, v0
	v_bfe_u32 v138, v0, 5, 1
	v_and_b32_e32 v142, 0xc0, v1
	v_lshlrev_b32_e32 v1, 7, v139
	v_and_b32_e32 v140, 31, v0
	v_and_b32_e32 v141, 0x80, v1
	v_or_b32_e32 v1, 2, v138
	s_and_b64 vcc, exec, s[14:15]
	s_cbranch_vccz .LBB5_20
	v_or_b32_e32 v2, v142, v140
	v_bitop3_b32 v4, v1, v11, 3 bitop3:0x78
	v_lshlrev_b32_e32 v144, 6, v2
	v_lshlrev_b32_e32 v146, 4, v4
	v_or_b32_e32 v2, v141, v140
	v_add_u32_e32 v4, s16, v11
	v_lshlrev_b32_e32 v147, 6, v2
	v_min_i32_e32 v2, s24, v4
	v_mul_lo_u32 v2, s6, v2
	v_bitop3_b32 v3, v138, v11, 3 bitop3:0x78
	v_add3_u32 v2, v2, s9, v10
	v_lshlrev_b32_e32 v145, 4, v3
	v_ashrrev_i32_e32 v3, 31, v2
	v_lshl_add_u64 v[2:3], v[2:3], 1, s[4:5]
	s_mov_b64 s[26:27], 0xc0
	v_lshl_add_u64 v[130:131], v[2:3], 0, s[26:27]
	v_add_u32_e32 v2, 0x80, v4
	v_min_i32_e32 v2, s24, v2
	v_mul_lo_u32 v2, s6, v2
	v_add3_u32 v2, v2, s9, v10
	v_ashrrev_i32_e32 v3, 31, v2
	s_mul_i32 s19, s19, s21
	v_lshl_add_u64 v[2:3], v[2:3], 1, s[4:5]
	s_sub_i32 s4, s22, s19
	s_sub_i32 s4, s4, s23
	s_mul_i32 s4, s10, s4
	s_lshl_b32 s4, s4, 8
	s_lshl_b32 s5, s20, 8
	s_add_i32 s5, s5, s4
	v_or_b32_e32 v4, s5, v11
	v_lshl_add_u64 v[132:133], v[2:3], 0, s[26:27]
	v_mul_lo_u32 v2, s8, v4
	v_add3_u32 v2, v2, s9, v10
	v_ashrrev_i32_e32 v3, 31, v2
	v_lshl_add_u64 v[2:3], v[2:3], 1, s[12:13]
	v_lshl_add_u64 v[134:135], v[2:3], 0, s[26:27]
	v_or_b32_e32 v2, 0x80, v4
	v_mul_lo_u32 v2, s8, v2
	v_add3_u32 v2, v2, s9, v10
	v_ashrrev_i32_e32 v3, 31, v2
	v_lshl_add_u64 v[2:3], v[2:3], 1, s[12:13]
	v_lshl_add_u64 v[136:137], v[2:3], 0, s[26:27]
	v_mov_b32_e32 v2, 0
	s_mov_b32 s14, 3
	s_add_i32 s15, s18, -1
	s_mov_b32 s6, 0
	s_mov_b64 s[4:5], 0
	s_mov_b32 s10, 3
	v_mov_b32_e32 v3, v2
	v_mov_b32_e32 v4, v2
	v_mov_b32_e32 v5, v2
	v_mov_b32_e32 v6, v2
	v_mov_b32_e32 v7, v2
	v_mov_b32_e32 v8, v2
	v_mov_b32_e32 v9, v2
	v_mov_b32_e32 v10, v2
	v_mov_b32_e32 v11, v2
	v_mov_b32_e32 v12, v2
	v_mov_b32_e32 v13, v2
	v_mov_b32_e32 v14, v2
	v_mov_b32_e32 v15, v2
	v_mov_b32_e32 v16, v2
	v_mov_b32_e32 v17, v2
	v_mov_b32_e32 v18, v2
	v_mov_b32_e32 v19, v2
	v_mov_b32_e32 v20, v2
	v_mov_b32_e32 v21, v2
	v_mov_b32_e32 v22, v2
	v_mov_b32_e32 v23, v2
	v_mov_b32_e32 v24, v2
	v_mov_b32_e32 v25, v2
	v_mov_b32_e32 v26, v2
	v_mov_b32_e32 v27, v2
	v_mov_b32_e32 v28, v2
	v_mov_b32_e32 v29, v2
	v_mov_b32_e32 v30, v2
	v_mov_b32_e32 v31, v2
	v_mov_b32_e32 v32, v2
	v_mov_b32_e32 v33, v2
	v_mov_b32_e32 v34, v2
	v_mov_b32_e32 v35, v2
	v_mov_b32_e32 v36, v2
	v_mov_b32_e32 v37, v2
	v_mov_b32_e32 v38, v2
	v_mov_b32_e32 v39, v2
	v_mov_b32_e32 v40, v2
	v_mov_b32_e32 v41, v2
	v_mov_b32_e32 v42, v2
	v_mov_b32_e32 v43, v2
	v_mov_b32_e32 v44, v2
	v_mov_b32_e32 v45, v2
	v_mov_b32_e32 v46, v2
	v_mov_b32_e32 v47, v2
	v_mov_b32_e32 v48, v2
	v_mov_b32_e32 v49, v2
	v_mov_b32_e32 v50, v2
	v_mov_b32_e32 v51, v2
	v_mov_b32_e32 v52, v2
	v_mov_b32_e32 v53, v2
	v_mov_b32_e32 v54, v2
	v_mov_b32_e32 v55, v2
	v_mov_b32_e32 v56, v2
	v_mov_b32_e32 v57, v2
	v_mov_b32_e32 v58, v2
	v_mov_b32_e32 v59, v2
	v_mov_b32_e32 v60, v2
	v_mov_b32_e32 v61, v2
	v_mov_b32_e32 v62, v2
	v_mov_b32_e32 v63, v2
	v_mov_b32_e32 v64, v2
	v_mov_b32_e32 v65, v2
	v_mov_b32_e32 v66, v2
	v_mov_b32_e32 v67, v2
	v_mov_b32_e32 v68, v2
	v_mov_b32_e32 v69, v2
	v_mov_b32_e32 v70, v2
	v_mov_b32_e32 v71, v2
	v_mov_b32_e32 v72, v2
	v_mov_b32_e32 v73, v2
	v_mov_b32_e32 v74, v2
	v_mov_b32_e32 v75, v2
	v_mov_b32_e32 v76, v2
	v_mov_b32_e32 v77, v2
	v_mov_b32_e32 v78, v2
	v_mov_b32_e32 v79, v2
	v_mov_b32_e32 v80, v2
	v_mov_b32_e32 v81, v2
	v_mov_b32_e32 v82, v2
	v_mov_b32_e32 v83, v2
	v_mov_b32_e32 v84, v2
	v_mov_b32_e32 v85, v2
	v_mov_b32_e32 v86, v2
	v_mov_b32_e32 v87, v2
	v_mov_b32_e32 v88, v2
	v_mov_b32_e32 v89, v2
	v_mov_b32_e32 v90, v2
	v_mov_b32_e32 v91, v2
	v_mov_b32_e32 v92, v2
	v_mov_b32_e32 v93, v2
	v_mov_b32_e32 v94, v2
	v_mov_b32_e32 v95, v2
	v_mov_b32_e32 v96, v2
	v_mov_b32_e32 v97, v2
	v_mov_b32_e32 v98, v2
	v_mov_b32_e32 v99, v2
	v_mov_b32_e32 v100, v2
	v_mov_b32_e32 v101, v2
	v_mov_b32_e32 v102, v2
	v_mov_b32_e32 v103, v2
	v_mov_b32_e32 v104, v2
	v_mov_b32_e32 v105, v2
	v_mov_b32_e32 v106, v2
	v_mov_b32_e32 v107, v2
	v_mov_b32_e32 v108, v2
	v_mov_b32_e32 v109, v2
	v_mov_b32_e32 v110, v2
	v_mov_b32_e32 v111, v2
	v_mov_b32_e32 v112, v2
	v_mov_b32_e32 v113, v2
	v_mov_b32_e32 v114, v2
	v_mov_b32_e32 v115, v2
	v_mov_b32_e32 v116, v2
	v_mov_b32_e32 v117, v2
	v_mov_b32_e32 v118, v2
	v_mov_b32_e32 v119, v2
	v_mov_b32_e32 v120, v2
	v_mov_b32_e32 v121, v2
	v_mov_b32_e32 v122, v2
	v_mov_b32_e32 v123, v2
	v_mov_b32_e32 v124, v2
	v_mov_b32_e32 v125, v2
	v_mov_b32_e32 v126, v2
	v_mov_b32_e32 v127, v2
	v_mov_b32_e32 v128, v2
	v_mov_b32_e32 v129, v2
	v_readfirstlane_b32 s28, v143
	v_add_u32_e32 v172, v144, v145
	v_add_u32_e32 v173, v144, v146
	v_add_u32_e32 v144, v147, v145
	v_add_u32_e32 v147, v147, v146
	v_mov_b32_e32 v145, v172
	v_mov_b32_e32 v146, v173
	s_mov_b32 s9, 0x18000
	s_or_b32 m0, s9, s28
	s_nop 0
	global_load_lds_dwordx4 v[130:131], off
	v_lshl_add_u64 v[130:131], v[130:131], 0, 64
	s_add_u32 m0, m0, 0x2000
	global_load_lds_dwordx4 v[132:133], off
	v_lshl_add_u64 v[132:133], v[132:133], 0, 64
	s_add_u32 m0, m0, 0x2000
	global_load_lds_dwordx4 v[134:135], off
	v_lshl_add_u64 v[134:135], v[134:135], 0, 64
	s_add_u32 m0, m0, 0x2000
	global_load_lds_dwordx4 v[136:137], off
	v_lshl_add_u64 v[136:137], v[136:137], 0, 64
	s_mov_b32 s10, 4
	s_waitcnt vmcnt(12)
	s_barrier
	s_cmp_ge_u32 s28, 0x1000
	s_cbranch_scc1 .Lk5_hi
	ds_read_b128 v[148:151], v145
	ds_read_b128 v[152:155], v144 offset:16384
	ds_read_b128 v[160:163], v144 offset:18432
	ds_read_b128 v[156:159], v145 offset:2048
	ds_read_b128 v[164:167], v144 offset:20480
	ds_read_b128 v[168:171], v144 offset:22528
	.p2align	6

.Lk5_hi:
	s_waitcnt vmcnt(8)
	s_waitcnt lgkmcnt(0)
	s_barrier
	s_lshl_b32 s8, s6, 15
	v_add_u32_e32 v174, s8, v145
	v_add_u32_e32 v175, s8, v144
	ds_read_b128 v[148:151], v174
	ds_read_b128 v[152:155], v175 offset:16384
	ds_read_b128 v[160:163], v175 offset:18432
	ds_read_b128 v[156:159], v174 offset:2048
	ds_read_b128 v[164:167], v175 offset:20480
	ds_read_b128 v[168:171], v175 offset:22528
	v_add_u32_e32 v172, s8, v146
	v_add_u32_e32 v173, s8, v147
	s_waitcnt lgkmcnt(0)
	ds_read_b128 v[176:179], v172
	ds_read_b128 v[184:187], v173 offset:16384
	ds_read_b128 v[188:191], v173 offset:18432
	ds_read_b128 v[180:183], v172 offset:2048
	ds_read_b128 v[192:195], v173 offset:20480
	ds_read_b128 v[196:199], v173 offset:22528
	s_lshl_b32 s9, s10, 15
	s_or_b32 m0, s9, s28
	v_mfma_f32_32x32x16_f16 v[114:129], v[148:151], v[152:155], v[114:129]
	global_load_lds_dwordx4 v[130:131], off
	v_lshl_add_u64 v[130:131], v[130:131], 0, 64
	s_add_u32 m0, m0, 0x2000
	v_mfma_f32_32x32x16_f16 v[98:113], v[148:151], v[160:163], v[98:113]
	global_load_lds_dwordx4 v[132:133], off
	v_lshl_add_u64 v[132:133], v[132:133], 0, 64
	s_add_u32 m0, m0, 0x2000
	v_mfma_f32_32x32x16_f16 v[82:97], v[148:151], v[164:167], v[82:97]
	global_load_lds_dwordx4 v[134:135], off
	v_lshl_add_u64 v[134:135], v[134:135], 0, 64
	s_add_u32 m0, m0, 0x2000
	v_mfma_f32_32x32x16_f16 v[66:81], v[148:151], v[168:171], v[66:81]
	global_load_lds_dwordx4 v[136:137], off
	v_lshl_add_u64 v[136:137], v[136:137], 0, 64
	v_mfma_f32_32x32x16_f16 v[50:65], v[156:159], v[152:155], v[50:65]
	v_mfma_f32_32x32x16_f16 v[34:49], v[156:159], v[160:163], v[34:49]
	v_mfma_f32_32x32x16_f16 v[18:33], v[156:159], v[164:167], v[18:33]
	v_mfma_f32_32x32x16_f16 v[2:17], v[156:159], v[168:171], v[2:17]
	s_add_i32 s6, s6, 1
	s_cmp_eq_u32 s6, 5
	s_cselect_b32 s6, 0, s6
	s_add_i32 s10, s10, 1
	s_cmp_eq_u32 s10, 5
	s_cselect_b32 s10, 0, s10
	.p2align	6
